# adds P4 and P8 K-loop LDS-DMA in SGPR-base form to the previous stack (all int8 K-loops + P14 without 64-bit VALU address adds)
# speedup vs baseline: 1.0020x; 1.0020x over previous
.LBB0_788:
	v_add_u32_e32 v130, s15, v190
	v_add_u32_e32 v134, s50, v190
	ds_read_b128 v[158:161], v130
	ds_read_b128 v[150:153], v130 offset:1024
	ds_read_b128 v[154:157], v130 offset:2048
	ds_read_b128 v[146:149], v130 offset:3072
	ds_read_b128 v[142:145], v134
	ds_read_b128 v[130:133], v134 offset:1024
	ds_read_b128 v[138:141], v134 offset:2048
	ds_read_b128 v[134:137], v134 offset:3072
	s_add_u32 s36, s34, 0xfff80080
	s_addc_u32 s37, s35, -1
	s_and_b64 s[0:1], s[0:1], exec
	s_cselect_b32 s39, s21, s37
	s_cselect_b32 s38, s60, s36
	s_cselect_b32 s37, s17, s63
	s_cselect_b32 s36, s61, s62
	s_add_i32 m0, s29, 0xc000
	ds_read_b128 v[182:185], v193
	ds_read_b128 v[186:189], v193 offset:1024
	ds_read_b128 v[194:197], v193 offset:2048
	ds_read_b128 v[198:201], v193 offset:3072
	ds_read_b128 v[202:205], v193 offset:4096
	ds_read_b128 v[206:209], v193 offset:5120
	ds_read_b128 v[210:213], v193 offset:6144
	ds_read_b128 v[214:217], v193 offset:7168
	global_load_lds_dwordx4 v172, s[34:35]
	s_add_i32 m0, s29, 0xe000
	s_nop 0
	global_load_lds_dwordx4 v174, s[34:35]
	s_waitcnt vmcnt(8)
	s_waitcnt lgkmcnt(0)
	s_barrier
	s_setprio 1
	s_waitcnt lgkmcnt(0)
	v_mfma_i32_16x16x64_i8 v[126:129], v[158:161], v[182:185], v[126:129]
	v_mfma_i32_16x16x64_i8 v[122:125], v[154:157], v[182:185], v[122:125]
	v_mfma_i32_16x16x64_i8 v[114:117], v[158:161], v[194:197], v[114:117]
	v_mfma_i32_16x16x64_i8 v[106:109], v[154:157], v[194:197], v[106:109]
	v_mfma_i32_16x16x64_i8 v[98:101], v[158:161], v[202:205], v[98:101]
	v_mfma_i32_16x16x64_i8 v[90:93], v[154:157], v[202:205], v[90:93]
	v_mfma_i32_16x16x64_i8 v[82:85], v[158:161], v[210:213], v[82:85]
	v_mfma_i32_16x16x64_i8 v[74:77], v[154:157], v[210:213], v[74:77]
	s_nop 0
	v_mfma_i32_16x16x64_i8 v[126:129], v[150:153], v[186:189], v[126:129]
	v_mfma_i32_16x16x64_i8 v[122:125], v[146:149], v[186:189], v[122:125]
	v_mfma_i32_16x16x64_i8 v[114:117], v[150:153], v[198:201], v[114:117]
	v_mfma_i32_16x16x64_i8 v[106:109], v[146:149], v[198:201], v[106:109]
	v_mfma_i32_16x16x64_i8 v[98:101], v[150:153], v[206:209], v[98:101]
	v_mfma_i32_16x16x64_i8 v[90:93], v[146:149], v[206:209], v[90:93]
	v_mfma_i32_16x16x64_i8 v[82:85], v[150:153], v[214:217], v[82:85]
	v_mfma_i32_16x16x64_i8 v[74:77], v[146:149], v[214:217], v[74:77]
	s_setprio 0
	s_setprio 1
	v_mfma_i32_16x16x64_i8 v[118:121], v[142:145], v[182:185], v[118:121]
	v_mfma_i32_16x16x64_i8 v[110:113], v[138:141], v[182:185], v[110:113]
	v_mfma_i32_16x16x64_i8 v[102:105], v[142:145], v[194:197], v[102:105]
	v_mfma_i32_16x16x64_i8 v[94:97], v[138:141], v[194:197], v[94:97]
	v_mfma_i32_16x16x64_i8 v[86:89], v[142:145], v[202:205], v[86:89]
	v_mfma_i32_16x16x64_i8 v[78:81], v[138:141], v[202:205], v[78:81]
	v_mfma_i32_16x16x64_i8 v[70:73], v[142:145], v[210:213], v[70:73]
	v_mfma_i32_16x16x64_i8 v[66:69], v[138:141], v[210:213], v[66:69]
	s_nop 0
	v_mfma_i32_16x16x64_i8 v[118:121], v[130:133], v[186:189], v[118:121]
	v_mfma_i32_16x16x64_i8 v[110:113], v[134:137], v[186:189], v[110:113]
	v_mfma_i32_16x16x64_i8 v[102:105], v[130:133], v[198:201], v[102:105]
	v_mfma_i32_16x16x64_i8 v[94:97], v[134:137], v[198:201], v[94:97]
	v_mfma_i32_16x16x64_i8 v[86:89], v[130:133], v[206:209], v[86:89]
	v_mfma_i32_16x16x64_i8 v[78:81], v[134:137], v[206:209], v[78:81]
	v_mfma_i32_16x16x64_i8 v[70:73], v[130:133], v[214:217], v[70:73]
	v_mfma_i32_16x16x64_i8 v[66:69], v[134:137], v[214:217], v[66:69]
	s_setprio 0
	s_barrier
	s_add_i32 s0, s15, s40
	s_mov_b32 m0, s0
	ds_read_b128 v[194:197], v193 offset:16384
	ds_read_b128 v[198:201], v193 offset:17408
	ds_read_b128 v[202:205], v193 offset:18432
	ds_read_b128 v[206:209], v193 offset:19456
	ds_read_b128 v[210:213], v193 offset:20480
	ds_read_b128 v[214:217], v193 offset:21504
	ds_read_b128 v[218:221], v193 offset:22528
	ds_read_b128 v[222:225], v193 offset:23552
	global_load_lds_dwordx4 v164, s[36:37]
	s_add_i32 m0, s0, 0x2000
	s_add_u32 s0, s36, 0x80000
	s_addc_u32 s1, s37, 0
	s_add_i32 s66, s50, s40
	global_load_lds_dwordx4 v168, s[36:37]
	s_mov_b32 m0, s66
	s_nop 0
	global_load_lds_dwordx4 v164, s[0:1]
	s_add_i32 m0, s66, 0x2000
	s_nop 0
	global_load_lds_dwordx4 v168, s[0:1]
	s_mov_b32 m0, s29
	s_nop 0
	global_load_lds_dwordx4 v162, s[38:39]
	s_mov_b32 m0, s31
	s_nop 0
	global_load_lds_dwordx4 v166, s[38:39]
	s_waitcnt vmcnt(8)
	s_waitcnt lgkmcnt(0)
	s_barrier
	s_setprio 1
	s_waitcnt lgkmcnt(0)
	v_mfma_i32_16x16x64_i8 v[62:65], v[158:161], v[194:197], v[62:65]
	v_mfma_i32_16x16x64_i8 v[58:61], v[154:157], v[194:197], v[58:61]
	v_mfma_i32_16x16x64_i8 v[50:53], v[158:161], v[202:205], v[50:53]
	v_mfma_i32_16x16x64_i8 v[42:45], v[154:157], v[202:205], v[42:45]
	v_mfma_i32_16x16x64_i8 v[34:37], v[158:161], v[210:213], v[34:37]
	v_mfma_i32_16x16x64_i8 v[26:29], v[154:157], v[210:213], v[26:29]
	v_mfma_i32_16x16x64_i8 v[18:21], v[158:161], v[218:221], v[18:21]
	v_mfma_i32_16x16x64_i8 v[10:13], v[154:157], v[218:221], v[10:13]
	s_nop 0
	v_mfma_i32_16x16x64_i8 v[62:65], v[150:153], v[198:201], v[62:65]
	v_mfma_i32_16x16x64_i8 v[58:61], v[146:149], v[198:201], v[58:61]
	v_mfma_i32_16x16x64_i8 v[50:53], v[150:153], v[206:209], v[50:53]
	v_mfma_i32_16x16x64_i8 v[42:45], v[146:149], v[206:209], v[42:45]
	v_mfma_i32_16x16x64_i8 v[34:37], v[150:153], v[214:217], v[34:37]
	v_mfma_i32_16x16x64_i8 v[26:29], v[146:149], v[214:217], v[26:29]
	v_mfma_i32_16x16x64_i8 v[18:21], v[150:153], v[222:225], v[18:21]
	v_mfma_i32_16x16x64_i8 v[10:13], v[146:149], v[222:225], v[10:13]
	s_setprio 0
	s_setprio 1
	v_mfma_i32_16x16x64_i8 v[54:57], v[142:145], v[194:197], v[54:57]
	v_mfma_i32_16x16x64_i8 v[46:49], v[138:141], v[194:197], v[46:49]
	v_mfma_i32_16x16x64_i8 v[38:41], v[142:145], v[202:205], v[38:41]
	v_mfma_i32_16x16x64_i8 v[30:33], v[138:141], v[202:205], v[30:33]
	v_mfma_i32_16x16x64_i8 v[22:25], v[142:145], v[210:213], v[22:25]
	v_mfma_i32_16x16x64_i8 v[14:17], v[138:141], v[210:213], v[14:17]
	v_mfma_i32_16x16x64_i8 v[6:9], v[142:145], v[218:221], v[6:9]
	v_mfma_i32_16x16x64_i8 v[2:5], v[138:141], v[218:221], v[2:5]
	s_nop 0
	v_mfma_i32_16x16x64_i8 v[54:57], v[130:133], v[198:201], v[54:57]
	v_mfma_i32_16x16x64_i8 v[46:49], v[134:137], v[198:201], v[46:49]
	v_mfma_i32_16x16x64_i8 v[38:41], v[130:133], v[206:209], v[38:41]
	v_mfma_i32_16x16x64_i8 v[30:33], v[134:137], v[206:209], v[30:33]
	v_mfma_i32_16x16x64_i8 v[22:25], v[130:133], v[214:217], v[22:25]
	v_mfma_i32_16x16x64_i8 v[14:17], v[134:137], v[214:217], v[14:17]
	v_mfma_i32_16x16x64_i8 v[6:9], v[130:133], v[222:225], v[6:9]
	v_mfma_i32_16x16x64_i8 v[2:5], v[134:137], v[222:225], v[2:5]
	s_setprio 0
	s_barrier
	s_add_i32 s66, 0, 0x18000
	s_add_i32 s67, 0, 0x1c000
	v_add_u32_e32 v142, s66, v190
	v_add_u32_e32 v158, s67, v190
	ds_read_b128 v[130:133], v142
	ds_read_b128 v[134:137], v142 offset:1024
	ds_read_b128 v[138:141], v142 offset:2048
	ds_read_b128 v[142:145], v142 offset:3072
	ds_read_b128 v[146:149], v158
	ds_read_b128 v[150:153], v158 offset:1024
	ds_read_b128 v[154:157], v158 offset:2048
	ds_read_b128 v[158:161], v158 offset:3072
	s_add_u32 s0, s38, 0x80000
	s_addc_u32 s1, s39, 0
	s_mov_b32 m0, s42
	ds_read_b128 v[194:197], v193 offset:32768
	ds_read_b128 v[198:201], v193 offset:33792
	ds_read_b128 v[202:205], v193 offset:34816
	ds_read_b128 v[206:209], v193 offset:35840
	ds_read_b128 v[210:213], v193 offset:36864
	ds_read_b128 v[214:217], v193 offset:37888
	ds_read_b128 v[218:221], v193 offset:38912
	ds_read_b128 v[222:225], v193 offset:39936
	global_load_lds_dwordx4 v162, s[0:1]
	s_mov_b32 m0, s43
	s_nop 0
	global_load_lds_dwordx4 v166, s[0:1]
	s_waitcnt vmcnt(8)
	s_waitcnt lgkmcnt(0)
	s_barrier
	s_setprio 1
	s_waitcnt lgkmcnt(0)
	v_mfma_i32_16x16x64_i8 v[126:129], v[130:133], v[194:197], v[126:129]
	v_mfma_i32_16x16x64_i8 v[122:125], v[138:141], v[194:197], v[122:125]
	v_mfma_i32_16x16x64_i8 v[114:117], v[130:133], v[202:205], v[114:117]
	v_mfma_i32_16x16x64_i8 v[106:109], v[138:141], v[202:205], v[106:109]
	v_mfma_i32_16x16x64_i8 v[98:101], v[130:133], v[210:213], v[98:101]
	v_mfma_i32_16x16x64_i8 v[90:93], v[138:141], v[210:213], v[90:93]
	v_mfma_i32_16x16x64_i8 v[82:85], v[130:133], v[218:221], v[82:85]
	v_mfma_i32_16x16x64_i8 v[74:77], v[138:141], v[218:221], v[74:77]
	s_nop 0
	v_mfma_i32_16x16x64_i8 v[126:129], v[134:137], v[198:201], v[126:129]
	v_mfma_i32_16x16x64_i8 v[122:125], v[142:145], v[198:201], v[122:125]
	v_mfma_i32_16x16x64_i8 v[114:117], v[134:137], v[206:209], v[114:117]
	v_mfma_i32_16x16x64_i8 v[106:109], v[142:145], v[206:209], v[106:109]
	v_mfma_i32_16x16x64_i8 v[98:101], v[134:137], v[214:217], v[98:101]
	v_mfma_i32_16x16x64_i8 v[90:93], v[142:145], v[214:217], v[90:93]
	v_mfma_i32_16x16x64_i8 v[82:85], v[134:137], v[222:225], v[82:85]
	v_mfma_i32_16x16x64_i8 v[74:77], v[142:145], v[222:225], v[74:77]
	s_setprio 0
	s_setprio 1
	v_mfma_i32_16x16x64_i8 v[118:121], v[146:149], v[194:197], v[118:121]
	v_mfma_i32_16x16x64_i8 v[110:113], v[154:157], v[194:197], v[110:113]
	v_mfma_i32_16x16x64_i8 v[102:105], v[146:149], v[202:205], v[102:105]
	v_mfma_i32_16x16x64_i8 v[94:97], v[154:157], v[202:205], v[94:97]
	v_mfma_i32_16x16x64_i8 v[86:89], v[146:149], v[210:213], v[86:89]
	v_mfma_i32_16x16x64_i8 v[78:81], v[154:157], v[210:213], v[78:81]
	v_mfma_i32_16x16x64_i8 v[70:73], v[146:149], v[218:221], v[70:73]
	v_mfma_i32_16x16x64_i8 v[66:69], v[154:157], v[218:221], v[66:69]
	s_nop 0
	v_mfma_i32_16x16x64_i8 v[118:121], v[150:153], v[198:201], v[118:121]
	v_mfma_i32_16x16x64_i8 v[110:113], v[158:161], v[198:201], v[110:113]
	v_mfma_i32_16x16x64_i8 v[102:105], v[150:153], v[206:209], v[102:105]
	v_mfma_i32_16x16x64_i8 v[94:97], v[158:161], v[206:209], v[94:97]
	v_mfma_i32_16x16x64_i8 v[86:89], v[150:153], v[214:217], v[86:89]
	v_mfma_i32_16x16x64_i8 v[78:81], v[158:161], v[214:217], v[78:81]
	v_mfma_i32_16x16x64_i8 v[70:73], v[150:153], v[222:225], v[70:73]
	v_mfma_i32_16x16x64_i8 v[66:69], v[158:161], v[222:225], v[66:69]
	s_setprio 0
	s_barrier
	s_add_i32 s0, s66, s40
	s_mov_b32 m0, s0
	s_add_u32 s98, s36, 0x80
	s_addc_u32 s99, s37, 0
	s_add_u32 s100, s38, 0x80
	s_addc_u32 s101, s39, 0
	ds_read_b128 v[194:197], v193 offset:49152
	ds_read_b128 v[198:201], v193 offset:50176
	ds_read_b128 v[202:205], v193 offset:51200
	ds_read_b128 v[206:209], v193 offset:52224
	ds_read_b128 v[210:213], v193 offset:53248
	ds_read_b128 v[214:217], v193 offset:54272
	ds_read_b128 v[218:221], v193 offset:55296
	ds_read_b128 v[222:225], v193 offset:56320
	global_load_lds_dwordx4 v164, s[98:99]
	s_add_i32 m0, s0, 0x2000
	s_add_u32 s0, s36, 0x80080
	s_addc_u32 s1, s37, 0
	s_add_i32 s36, s67, s40
	global_load_lds_dwordx4 v168, s[98:99]
	s_mov_b32 m0, s36
	s_nop 0
	global_load_lds_dwordx4 v164, s[0:1]
	s_add_i32 m0, s36, 0x2000
	s_nop 0
	global_load_lds_dwordx4 v168, s[0:1]
	s_mov_b32 m0, s48
	s_nop 0
	global_load_lds_dwordx4 v162, s[100:101]
	s_mov_b32 m0, s49
	s_nop 0
	global_load_lds_dwordx4 v166, s[100:101]
	s_waitcnt vmcnt(8)
	s_waitcnt lgkmcnt(0)
	s_barrier
	s_setprio 1
	s_waitcnt lgkmcnt(0)
	v_mfma_i32_16x16x64_i8 v[62:65], v[130:133], v[194:197], v[62:65]
	v_mfma_i32_16x16x64_i8 v[58:61], v[138:141], v[194:197], v[58:61]
	v_mfma_i32_16x16x64_i8 v[50:53], v[130:133], v[202:205], v[50:53]
	v_mfma_i32_16x16x64_i8 v[42:45], v[138:141], v[202:205], v[42:45]
	v_mfma_i32_16x16x64_i8 v[34:37], v[130:133], v[210:213], v[34:37]
	v_mfma_i32_16x16x64_i8 v[26:29], v[138:141], v[210:213], v[26:29]
	v_mfma_i32_16x16x64_i8 v[18:21], v[130:133], v[218:221], v[18:21]
	v_mfma_i32_16x16x64_i8 v[10:13], v[138:141], v[218:221], v[10:13]
	s_nop 0
	v_mfma_i32_16x16x64_i8 v[62:65], v[134:137], v[198:201], v[62:65]
	v_mfma_i32_16x16x64_i8 v[58:61], v[142:145], v[198:201], v[58:61]
	v_mfma_i32_16x16x64_i8 v[50:53], v[134:137], v[206:209], v[50:53]
	v_mfma_i32_16x16x64_i8 v[42:45], v[142:145], v[206:209], v[42:45]
	v_mfma_i32_16x16x64_i8 v[34:37], v[134:137], v[214:217], v[34:37]
	v_mfma_i32_16x16x64_i8 v[26:29], v[142:145], v[214:217], v[26:29]
	v_mfma_i32_16x16x64_i8 v[18:21], v[134:137], v[222:225], v[18:21]
	v_mfma_i32_16x16x64_i8 v[10:13], v[142:145], v[222:225], v[10:13]
	s_setprio 0
	s_setprio 1
	v_mfma_i32_16x16x64_i8 v[54:57], v[146:149], v[194:197], v[54:57]
	v_mfma_i32_16x16x64_i8 v[46:49], v[154:157], v[194:197], v[46:49]
	v_mfma_i32_16x16x64_i8 v[38:41], v[146:149], v[202:205], v[38:41]
	v_mfma_i32_16x16x64_i8 v[30:33], v[154:157], v[202:205], v[30:33]
	v_mfma_i32_16x16x64_i8 v[22:25], v[146:149], v[210:213], v[22:25]
	v_mfma_i32_16x16x64_i8 v[14:17], v[154:157], v[210:213], v[14:17]
	v_mfma_i32_16x16x64_i8 v[6:9], v[146:149], v[218:221], v[6:9]
	v_mfma_i32_16x16x64_i8 v[2:5], v[154:157], v[218:221], v[2:5]
	s_nop 0
	v_mfma_i32_16x16x64_i8 v[54:57], v[150:153], v[198:201], v[54:57]
	v_mfma_i32_16x16x64_i8 v[46:49], v[158:161], v[198:201], v[46:49]
	v_mfma_i32_16x16x64_i8 v[38:41], v[150:153], v[206:209], v[38:41]
	v_mfma_i32_16x16x64_i8 v[30:33], v[158:161], v[206:209], v[30:33]
	v_mfma_i32_16x16x64_i8 v[22:25], v[150:153], v[214:217], v[22:25]
	v_mfma_i32_16x16x64_i8 v[14:17], v[158:161], v[214:217], v[14:17]
	v_mfma_i32_16x16x64_i8 v[6:9], v[150:153], v[222:225], v[6:9]
	v_mfma_i32_16x16x64_i8 v[2:5], v[158:161], v[222:225], v[2:5]
	s_setprio 0
	s_barrier
	s_add_i32 s64, s64, 2
	s_add_u32 s34, s34, 0x100
	s_addc_u32 s35, s35, 0
	s_add_u32 s62, s62, 0x100
	s_addc_u32 s63, s63, 0
	s_cmp_gt_u32 s64, 29
	s_cbranch_scc1 .LBB0_791

.LBB0_1051:
	s_add_u32 s8, s17, s6
	s_addc_u32 s9, s48, s7
	s_add_u32 s8, s8, 0x32800100
	s_addc_u32 s9, s9, 0
	s_add_u32 s65, s49, s6
	s_addc_u32 s68, s50, s7
	s_add_i32 s69, 0, 0x10000
	s_cmpk_eq_i32 s6, 0xf00
	s_cselect_b32 s41, s5, s9
	s_cselect_b32 s40, s4, s8
	s_cselect_b32 s9, s21, s68
	s_cselect_b32 s8, s20, s65
	s_add_i32 s65, 0, 0x14000
	v_add_u32_e32 v130, s69, v187
	v_add_u32_e32 v134, s65, v187
	ds_read_b128 v[158:161], v130
	ds_read_b128 v[150:153], v130 offset:1024
	ds_read_b128 v[154:157], v130 offset:2048
	ds_read_b128 v[146:149], v130 offset:3072
	ds_read_b128 v[142:145], v134
	ds_read_b128 v[130:133], v134 offset:1024
	ds_read_b128 v[138:141], v134 offset:2048
	ds_read_b128 v[134:137], v134 offset:3072
	v_lshl_add_u64 v[214:215], v[168:169], 0, s[6:7]
	s_add_i32 m0, s43, 0xc000
	ds_read_b128 v[172:175], v188
	ds_read_b128 v[176:179], v188 offset:1024
	ds_read_b128 v[190:193], v188 offset:2048
	ds_read_b128 v[194:197], v188 offset:3072
	ds_read_b128 v[198:201], v188 offset:4096
	ds_read_b128 v[202:205], v188 offset:5120
	ds_read_b128 v[206:209], v188 offset:6144
	ds_read_b128 v[210:213], v188 offset:7168
	global_load_lds_dwordx4 v[214:215], off
	v_lshl_add_u64 v[214:215], v[170:171], 0, s[6:7]
	s_add_i32 m0, s43, 0xe000
	s_nop 0
	global_load_lds_dwordx4 v[214:215], off
	s_waitcnt vmcnt(8)
	s_waitcnt lgkmcnt(0)
	s_barrier
	s_setprio 1
	s_waitcnt lgkmcnt(0)
	v_mfma_i32_16x16x64_i8 v[70:73], v[158:161], v[172:175], v[70:73]
	v_mfma_i32_16x16x64_i8 v[34:37], v[154:157], v[172:175], v[34:37]
	v_mfma_i32_16x16x64_i8 v[102:105], v[158:161], v[190:193], v[102:105]
	v_mfma_i32_16x16x64_i8 v[54:57], v[154:157], v[190:193], v[54:57]
	v_mfma_i32_16x16x64_i8 v[114:117], v[158:161], v[198:201], v[114:117]
	v_mfma_i32_16x16x64_i8 v[86:89], v[154:157], v[198:201], v[86:89]
	v_mfma_i32_16x16x64_i8 v[126:129], v[158:161], v[206:209], v[126:129]
	v_mfma_i32_16x16x64_i8 v[110:113], v[154:157], v[206:209], v[110:113]
	s_nop 0
	v_mfma_i32_16x16x64_i8 v[70:73], v[150:153], v[176:179], v[70:73]
	v_mfma_i32_16x16x64_i8 v[34:37], v[146:149], v[176:179], v[34:37]
	v_mfma_i32_16x16x64_i8 v[102:105], v[150:153], v[194:197], v[102:105]
	v_mfma_i32_16x16x64_i8 v[54:57], v[146:149], v[194:197], v[54:57]
	v_mfma_i32_16x16x64_i8 v[114:117], v[150:153], v[202:205], v[114:117]
	v_mfma_i32_16x16x64_i8 v[86:89], v[146:149], v[202:205], v[86:89]
	v_mfma_i32_16x16x64_i8 v[126:129], v[150:153], v[210:213], v[126:129]
	v_mfma_i32_16x16x64_i8 v[110:113], v[146:149], v[210:213], v[110:113]
	s_setprio 0
	s_setprio 1
	v_mfma_i32_16x16x64_i8 v[18:21], v[142:145], v[172:175], v[18:21]
	v_mfma_i32_16x16x64_i8 v[2:5], v[138:141], v[172:175], v[2:5]
	v_mfma_i32_16x16x64_i8 v[38:41], v[142:145], v[190:193], v[38:41]
	v_mfma_i32_16x16x64_i8 v[6:9], v[138:141], v[190:193], v[6:9]
	v_mfma_i32_16x16x64_i8 v[66:69], v[142:145], v[198:201], v[66:69]
	v_mfma_i32_16x16x64_i8 v[26:29], v[138:141], v[198:201], v[26:29]
	v_mfma_i32_16x16x64_i8 v[90:93], v[142:145], v[206:209], v[90:93]
	v_mfma_i32_16x16x64_i8 v[50:53], v[138:141], v[206:209], v[50:53]
	s_nop 0
	v_mfma_i32_16x16x64_i8 v[18:21], v[130:133], v[176:179], v[18:21]
	v_mfma_i32_16x16x64_i8 v[2:5], v[134:137], v[176:179], v[2:5]
	v_mfma_i32_16x16x64_i8 v[38:41], v[130:133], v[194:197], v[38:41]
	v_mfma_i32_16x16x64_i8 v[6:9], v[134:137], v[194:197], v[6:9]
	v_mfma_i32_16x16x64_i8 v[66:69], v[130:133], v[202:205], v[66:69]
	v_mfma_i32_16x16x64_i8 v[26:29], v[134:137], v[202:205], v[26:29]
	v_mfma_i32_16x16x64_i8 v[90:93], v[130:133], v[210:213], v[90:93]
	v_mfma_i32_16x16x64_i8 v[50:53], v[134:137], v[210:213], v[50:53]
	s_setprio 0
	s_barrier
	s_add_i32 s68, s69, s42
	s_mov_b32 m0, s68
	ds_read_b128 v[190:193], v188 offset:16384
	ds_read_b128 v[194:197], v188 offset:17408
	ds_read_b128 v[198:201], v188 offset:18432
	ds_read_b128 v[202:205], v188 offset:19456
	ds_read_b128 v[206:209], v188 offset:20480
	ds_read_b128 v[210:213], v188 offset:21504
	ds_read_b128 v[214:217], v188 offset:22528
	ds_read_b128 v[218:221], v188 offset:23552
	global_load_lds_dwordx4 v162, s[8:9]
	s_add_i32 m0, s68, 0x2000
	s_add_u32 s68, s8, 0x80000
	s_addc_u32 s69, s9, 0
	s_add_i32 s65, s65, s42
	global_load_lds_dwordx4 v166, s[8:9]
	s_mov_b32 m0, s65
	s_nop 0
	global_load_lds_dwordx4 v162, s[68:69]
	s_add_i32 m0, s65, 0x2000
	s_nop 0
	global_load_lds_dwordx4 v166, s[68:69]
	s_mov_b32 m0, s43
	s_nop 0
	global_load_lds_dwordx4 v162, s[40:41]
	s_mov_b32 m0, s60
	s_nop 0
	global_load_lds_dwordx4 v166, s[40:41]
	s_waitcnt vmcnt(8)
	s_waitcnt lgkmcnt(0)
	s_barrier
	s_setprio 1
	s_waitcnt lgkmcnt(0)
	v_mfma_i32_16x16x64_i8 v[122:125], v[158:161], v[190:193], v[122:125]
	v_mfma_i32_16x16x64_i8 v[118:121], v[154:157], v[190:193], v[118:121]
	v_mfma_i32_16x16x64_i8 v[98:101], v[158:161], v[198:201], v[98:101]
	v_mfma_i32_16x16x64_i8 v[94:97], v[154:157], v[198:201], v[94:97]
	v_mfma_i32_16x16x64_i8 v[62:65], v[158:161], v[206:209], v[62:65]
	v_mfma_i32_16x16x64_i8 v[58:61], v[154:157], v[206:209], v[58:61]
	v_mfma_i32_16x16x64_i8 v[30:33], v[158:161], v[214:217], v[30:33]
	v_mfma_i32_16x16x64_i8 v[22:25], v[154:157], v[214:217], v[22:25]
	s_nop 0
	v_mfma_i32_16x16x64_i8 v[122:125], v[150:153], v[194:197], v[122:125]
	v_mfma_i32_16x16x64_i8 v[118:121], v[146:149], v[194:197], v[118:121]
	v_mfma_i32_16x16x64_i8 v[98:101], v[150:153], v[202:205], v[98:101]
	v_mfma_i32_16x16x64_i8 v[94:97], v[146:149], v[202:205], v[94:97]
	v_mfma_i32_16x16x64_i8 v[62:65], v[150:153], v[210:213], v[62:65]
	v_mfma_i32_16x16x64_i8 v[58:61], v[146:149], v[210:213], v[58:61]
	v_mfma_i32_16x16x64_i8 v[30:33], v[150:153], v[218:221], v[30:33]
	v_mfma_i32_16x16x64_i8 v[22:25], v[146:149], v[218:221], v[22:25]
	s_setprio 0
	s_setprio 1
	v_mfma_i32_16x16x64_i8 v[106:109], v[142:145], v[190:193], v[106:109]
	v_mfma_i32_16x16x64_i8 v[82:85], v[138:141], v[190:193], v[82:85]
	v_mfma_i32_16x16x64_i8 v[78:81], v[142:145], v[198:201], v[78:81]
	v_mfma_i32_16x16x64_i8 v[74:77], v[138:141], v[198:201], v[74:77]
	v_mfma_i32_16x16x64_i8 v[46:49], v[142:145], v[206:209], v[46:49]
	v_mfma_i32_16x16x64_i8 v[42:45], v[138:141], v[206:209], v[42:45]
	v_mfma_i32_16x16x64_i8 v[14:17], v[142:145], v[214:217], v[14:17]
	v_mfma_i32_16x16x64_i8 v[10:13], v[138:141], v[214:217], v[10:13]
	s_nop 0
	v_mfma_i32_16x16x64_i8 v[106:109], v[130:133], v[194:197], v[106:109]
	v_mfma_i32_16x16x64_i8 v[82:85], v[134:137], v[194:197], v[82:85]
	v_mfma_i32_16x16x64_i8 v[78:81], v[130:133], v[202:205], v[78:81]
	v_mfma_i32_16x16x64_i8 v[74:77], v[134:137], v[202:205], v[74:77]
	v_mfma_i32_16x16x64_i8 v[46:49], v[130:133], v[210:213], v[46:49]
	v_mfma_i32_16x16x64_i8 v[42:45], v[134:137], v[210:213], v[42:45]
	v_mfma_i32_16x16x64_i8 v[14:17], v[130:133], v[218:221], v[14:17]
	v_mfma_i32_16x16x64_i8 v[10:13], v[134:137], v[218:221], v[10:13]
	s_setprio 0
	s_barrier
	s_add_i32 s65, 0, 0x18000
	s_add_i32 s68, 0, 0x1c000
	v_add_u32_e32 v142, s65, v187
	v_add_u32_e32 v158, s68, v187
	ds_read_b128 v[130:133], v142
	ds_read_b128 v[134:137], v142 offset:1024
	ds_read_b128 v[138:141], v142 offset:2048
	ds_read_b128 v[142:145], v142 offset:3072
	ds_read_b128 v[146:149], v158
	ds_read_b128 v[150:153], v158 offset:1024
	ds_read_b128 v[154:157], v158 offset:2048
	ds_read_b128 v[158:161], v158 offset:3072
	s_add_u32 s40, s40, 0x80000
	s_addc_u32 s41, s41, 0
	s_add_u32 s100, s40, 0xfff80080
	s_addc_u32 s101, s41, -1
	s_mov_b32 m0, s61
	ds_read_b128 v[190:193], v188 offset:32768
	ds_read_b128 v[194:197], v188 offset:33792
	ds_read_b128 v[198:201], v188 offset:34816
	ds_read_b128 v[202:205], v188 offset:35840
	ds_read_b128 v[206:209], v188 offset:36864
	ds_read_b128 v[210:213], v188 offset:37888
	ds_read_b128 v[214:217], v188 offset:38912
	ds_read_b128 v[218:221], v188 offset:39936
	global_load_lds_dwordx4 v162, s[40:41]
	s_mov_b32 m0, s62
	s_nop 0
	global_load_lds_dwordx4 v166, s[40:41]
	s_waitcnt vmcnt(8)
	s_waitcnt lgkmcnt(0)
	s_barrier
	s_setprio 1
	s_waitcnt lgkmcnt(0)
	v_mfma_i32_16x16x64_i8 v[70:73], v[130:133], v[190:193], v[70:73]
	v_mfma_i32_16x16x64_i8 v[34:37], v[138:141], v[190:193], v[34:37]
	v_mfma_i32_16x16x64_i8 v[102:105], v[130:133], v[198:201], v[102:105]
	v_mfma_i32_16x16x64_i8 v[54:57], v[138:141], v[198:201], v[54:57]
	v_mfma_i32_16x16x64_i8 v[114:117], v[130:133], v[206:209], v[114:117]
	v_mfma_i32_16x16x64_i8 v[86:89], v[138:141], v[206:209], v[86:89]
	v_mfma_i32_16x16x64_i8 v[126:129], v[130:133], v[214:217], v[126:129]
	v_mfma_i32_16x16x64_i8 v[110:113], v[138:141], v[214:217], v[110:113]
	s_nop 0
	v_mfma_i32_16x16x64_i8 v[70:73], v[134:137], v[194:197], v[70:73]
	v_mfma_i32_16x16x64_i8 v[34:37], v[142:145], v[194:197], v[34:37]
	v_mfma_i32_16x16x64_i8 v[102:105], v[134:137], v[202:205], v[102:105]
	v_mfma_i32_16x16x64_i8 v[54:57], v[142:145], v[202:205], v[54:57]
	v_mfma_i32_16x16x64_i8 v[114:117], v[134:137], v[210:213], v[114:117]
	v_mfma_i32_16x16x64_i8 v[86:89], v[142:145], v[210:213], v[86:89]
	v_mfma_i32_16x16x64_i8 v[126:129], v[134:137], v[218:221], v[126:129]
	v_mfma_i32_16x16x64_i8 v[110:113], v[142:145], v[218:221], v[110:113]
	s_setprio 0
	s_setprio 1
	v_mfma_i32_16x16x64_i8 v[18:21], v[146:149], v[190:193], v[18:21]
	v_mfma_i32_16x16x64_i8 v[2:5], v[154:157], v[190:193], v[2:5]
	v_mfma_i32_16x16x64_i8 v[38:41], v[146:149], v[198:201], v[38:41]
	v_mfma_i32_16x16x64_i8 v[6:9], v[154:157], v[198:201], v[6:9]
	v_mfma_i32_16x16x64_i8 v[66:69], v[146:149], v[206:209], v[66:69]
	v_mfma_i32_16x16x64_i8 v[26:29], v[154:157], v[206:209], v[26:29]
	v_mfma_i32_16x16x64_i8 v[90:93], v[146:149], v[214:217], v[90:93]
	v_mfma_i32_16x16x64_i8 v[50:53], v[154:157], v[214:217], v[50:53]
	s_nop 0
	v_mfma_i32_16x16x64_i8 v[18:21], v[150:153], v[194:197], v[18:21]
	v_mfma_i32_16x16x64_i8 v[2:5], v[158:161], v[194:197], v[2:5]
	v_mfma_i32_16x16x64_i8 v[38:41], v[150:153], v[202:205], v[38:41]
	v_mfma_i32_16x16x64_i8 v[6:9], v[158:161], v[202:205], v[6:9]
	v_mfma_i32_16x16x64_i8 v[66:69], v[150:153], v[210:213], v[66:69]
	v_mfma_i32_16x16x64_i8 v[26:29], v[158:161], v[210:213], v[26:29]
	v_mfma_i32_16x16x64_i8 v[90:93], v[150:153], v[218:221], v[90:93]
	v_mfma_i32_16x16x64_i8 v[50:53], v[158:161], v[218:221], v[50:53]
	s_setprio 0
	s_barrier
	s_add_i32 s40, s65, s42
	s_mov_b32 m0, s40
	s_add_u32 s98, s8, 0x80
	s_addc_u32 s99, s9, 0
	ds_read_b128 v[190:193], v188 offset:49152
	ds_read_b128 v[194:197], v188 offset:50176
	ds_read_b128 v[198:201], v188 offset:51200
	ds_read_b128 v[202:205], v188 offset:52224
	ds_read_b128 v[206:209], v188 offset:53248
	ds_read_b128 v[210:213], v188 offset:54272
	ds_read_b128 v[214:217], v188 offset:55296
	ds_read_b128 v[218:221], v188 offset:56320
	global_load_lds_dwordx4 v162, s[98:99]
	s_add_i32 m0, s40, 0x2000
	s_add_u32 s8, s8, 0x80080
	s_addc_u32 s9, s9, 0
	s_add_i32 s40, s68, s42
	global_load_lds_dwordx4 v166, s[98:99]
	s_mov_b32 m0, s40
	s_nop 0
	global_load_lds_dwordx4 v162, s[8:9]
	s_add_i32 m0, s40, 0x2000
	s_nop 0
	global_load_lds_dwordx4 v166, s[8:9]
	s_mov_b32 m0, s66
	s_nop 0
	global_load_lds_dwordx4 v162, s[100:101]
	s_mov_b32 m0, s67
	s_nop 0
	global_load_lds_dwordx4 v166, s[100:101]
	s_waitcnt vmcnt(8)
	s_waitcnt lgkmcnt(0)
	s_barrier
	s_setprio 1
	s_waitcnt lgkmcnt(0)
	v_mfma_i32_16x16x64_i8 v[122:125], v[130:133], v[190:193], v[122:125]
	v_mfma_i32_16x16x64_i8 v[118:121], v[138:141], v[190:193], v[118:121]
	v_mfma_i32_16x16x64_i8 v[98:101], v[130:133], v[198:201], v[98:101]
	v_mfma_i32_16x16x64_i8 v[94:97], v[138:141], v[198:201], v[94:97]
	v_mfma_i32_16x16x64_i8 v[62:65], v[130:133], v[206:209], v[62:65]
	v_mfma_i32_16x16x64_i8 v[58:61], v[138:141], v[206:209], v[58:61]
	v_mfma_i32_16x16x64_i8 v[30:33], v[130:133], v[214:217], v[30:33]
	v_mfma_i32_16x16x64_i8 v[22:25], v[138:141], v[214:217], v[22:25]
	s_nop 0
	v_mfma_i32_16x16x64_i8 v[122:125], v[134:137], v[194:197], v[122:125]
	v_mfma_i32_16x16x64_i8 v[118:121], v[142:145], v[194:197], v[118:121]
	v_mfma_i32_16x16x64_i8 v[98:101], v[134:137], v[202:205], v[98:101]
	v_mfma_i32_16x16x64_i8 v[94:97], v[142:145], v[202:205], v[94:97]
	v_mfma_i32_16x16x64_i8 v[62:65], v[134:137], v[210:213], v[62:65]
	v_mfma_i32_16x16x64_i8 v[58:61], v[142:145], v[210:213], v[58:61]
	v_mfma_i32_16x16x64_i8 v[30:33], v[134:137], v[218:221], v[30:33]
	v_mfma_i32_16x16x64_i8 v[22:25], v[142:145], v[218:221], v[22:25]
	s_setprio 0
	s_setprio 1
	v_mfma_i32_16x16x64_i8 v[106:109], v[146:149], v[190:193], v[106:109]
	v_mfma_i32_16x16x64_i8 v[82:85], v[154:157], v[190:193], v[82:85]
	v_mfma_i32_16x16x64_i8 v[78:81], v[146:149], v[198:201], v[78:81]
	v_mfma_i32_16x16x64_i8 v[74:77], v[154:157], v[198:201], v[74:77]
	v_mfma_i32_16x16x64_i8 v[46:49], v[146:149], v[206:209], v[46:49]
	v_mfma_i32_16x16x64_i8 v[42:45], v[154:157], v[206:209], v[42:45]
	v_mfma_i32_16x16x64_i8 v[14:17], v[146:149], v[214:217], v[14:17]
	v_mfma_i32_16x16x64_i8 v[10:13], v[154:157], v[214:217], v[10:13]
	s_nop 0
	v_mfma_i32_16x16x64_i8 v[106:109], v[150:153], v[194:197], v[106:109]
	v_mfma_i32_16x16x64_i8 v[82:85], v[158:161], v[194:197], v[82:85]
	v_mfma_i32_16x16x64_i8 v[78:81], v[150:153], v[202:205], v[78:81]
	v_mfma_i32_16x16x64_i8 v[74:77], v[158:161], v[202:205], v[74:77]
	v_mfma_i32_16x16x64_i8 v[46:49], v[150:153], v[210:213], v[46:49]
	v_mfma_i32_16x16x64_i8 v[42:45], v[158:161], v[210:213], v[42:45]
	v_mfma_i32_16x16x64_i8 v[14:17], v[150:153], v[218:221], v[14:17]
	v_mfma_i32_16x16x64_i8 v[10:13], v[158:161], v[218:221], v[10:13]
	s_setprio 0
	s_barrier
	s_add_i32 s64, s64, 2
	s_add_u32 s6, s6, 0x100
	s_addc_u32 s7, s7, 0
	s_cmp_gt_u32 s64, 29
	s_cbranch_scc0 .LBB0_1051
	s_waitcnt vmcnt(0)
	s_cmpk_lt_u32 s59, 0x100
	s_cbranch_scc0 .LBB0_1054
	s_barrier
